# plus: stream-A loop keeps the O accumulators in one register set (no 32 v_mov_b64 copies + s_nop 10 per tile)
# baseline (speedup 1.0000x reference)
;     ...
;     const bool rb = fin && (mx > 8.f || st.fresh);
;     if (__any(rb)) { const float d = rb ? mx : 0.f; const float corr = st.fresh ? 1.f : __builtin_amdgcn_exp2f(-d); st.l *= corr; st.m += d;
; #pragma unroll
;         for (int i = 0; i < 16; ++i) { st.O[0][i] *= corr; st.O[1][i] *= corr; S0[i] -= d; S1[i] -= d; }
;         if (IMP) { if (h == 0 && corr != 1.f) { for (int j = 0; j < 64; ++j) irow[j] *= corr; } }
;     }
.LBB0_564:
	s_or_b64 exec, exec, s[30:31]
	v_cndmask_b32_e64 v1, 0, 1, s[26:27]
	v_cmp_ne_u32_e32 vcc, 0, v1
	v_mov_b32_e32 v1, v224
	v_mov_b32_e32 v226, v225
	s_cbranch_vccz .LBB0_566
	v_cndmask_b32_e64 v14, 0, v14, s[26:27]
	v_exp_f32_e64 v1, -v14
	v_add_f32_e32 v226, v225, v14
	v_pk_add_f32 v[96:97], v[96:97], v[14:15] op_sel_hi:[1,0] neg_lo:[0,1] neg_hi:[0,1]
	v_pk_add_f32 v[80:81], v[80:81], v[14:15] op_sel_hi:[1,0] neg_lo:[0,1] neg_hi:[0,1]
	v_cndmask_b32_e64 v64, v1, 1.0, s[28:29]
	v_mul_f32_e32 v1, v224, v64
	v_pk_add_f32 v[98:99], v[98:99], v[14:15] op_sel_hi:[1,0] neg_lo:[0,1] neg_hi:[0,1]
	v_pk_add_f32 v[82:83], v[82:83], v[14:15] op_sel_hi:[1,0] neg_lo:[0,1] neg_hi:[0,1]
	v_pk_add_f32 v[100:101], v[100:101], v[14:15] op_sel_hi:[1,0] neg_lo:[0,1] neg_hi:[0,1]
	v_pk_add_f32 v[84:85], v[84:85], v[14:15] op_sel_hi:[1,0] neg_lo:[0,1] neg_hi:[0,1]
	v_pk_add_f32 v[102:103], v[102:103], v[14:15] op_sel_hi:[1,0] neg_lo:[0,1] neg_hi:[0,1]
	v_pk_add_f32 v[86:87], v[86:87], v[14:15] op_sel_hi:[1,0] neg_lo:[0,1] neg_hi:[0,1]
	v_pk_add_f32 v[104:105], v[104:105], v[14:15] op_sel_hi:[1,0] neg_lo:[0,1] neg_hi:[0,1]
	v_pk_add_f32 v[88:89], v[88:89], v[14:15] op_sel_hi:[1,0] neg_lo:[0,1] neg_hi:[0,1]
	v_pk_add_f32 v[106:107], v[106:107], v[14:15] op_sel_hi:[1,0] neg_lo:[0,1] neg_hi:[0,1]
	v_pk_add_f32 v[90:91], v[90:91], v[14:15] op_sel_hi:[1,0] neg_lo:[0,1] neg_hi:[0,1]
	v_pk_add_f32 v[108:109], v[108:109], v[14:15] op_sel_hi:[1,0] neg_lo:[0,1] neg_hi:[0,1]
	v_pk_add_f32 v[92:93], v[92:93], v[14:15] op_sel_hi:[1,0] neg_lo:[0,1] neg_hi:[0,1]
	v_pk_mul_f32 v[30:31], v[30:31], v[64:65] op_sel_hi:[1,0]
	v_pk_mul_f32 v[28:29], v[28:29], v[64:65] op_sel_hi:[1,0]
	v_pk_mul_f32 v[26:27], v[26:27], v[64:65] op_sel_hi:[1,0]
	v_pk_mul_f32 v[24:25], v[24:25], v[64:65] op_sel_hi:[1,0]
	v_pk_mul_f32 v[22:23], v[22:23], v[64:65] op_sel_hi:[1,0]
	v_pk_mul_f32 v[20:21], v[20:21], v[64:65] op_sel_hi:[1,0]
	v_pk_mul_f32 v[18:19], v[18:19], v[64:65] op_sel_hi:[1,0]
	v_pk_mul_f32 v[16:17], v[16:17], v[64:65] op_sel_hi:[1,0]
	v_pk_mul_f32 v[46:47], v[46:47], v[64:65] op_sel_hi:[1,0]
	v_pk_mul_f32 v[44:45], v[44:45], v[64:65] op_sel_hi:[1,0]
	v_pk_mul_f32 v[42:43], v[42:43], v[64:65] op_sel_hi:[1,0]
	v_pk_mul_f32 v[40:41], v[40:41], v[64:65] op_sel_hi:[1,0]
	v_pk_mul_f32 v[38:39], v[38:39], v[64:65] op_sel_hi:[1,0]
	v_pk_mul_f32 v[36:37], v[36:37], v[64:65] op_sel_hi:[1,0]
	v_pk_mul_f32 v[34:35], v[34:35], v[64:65] op_sel_hi:[1,0]
	v_pk_mul_f32 v[32:33], v[32:33], v[64:65] op_sel_hi:[1,0]
	v_pk_add_f32 v[110:111], v[110:111], v[14:15] op_sel_hi:[1,0] neg_lo:[0,1] neg_hi:[0,1]
	v_pk_add_f32 v[94:95], v[94:95], v[14:15] op_sel_hi:[1,0] neg_lo:[0,1] neg_hi:[0,1]
; __device__ __forceinline__ float xhalf_sum(float m) { float a, b; xhalf_pair(m, a, b); return a + b; }
;     ...
;     float ps = 0.f, pt = 0.f;
; #pragma unroll
;     for (int i = 0; i < 16; ++i) { S0[i] = __builtin_amdgcn_exp2f(S0[i]); S1[i] = __builtin_amdgcn_exp2f(S1[i]); ps += S0[i]; asm volatile("" : "+v"(ps)); pt += S1[i]; asm volatile("" : "+v"(pt)); }
;     st.l += ps + pt;
;     if (IMP) {
;         float prev3 = 0.f; const int partner = (lane ^ 32) << 2;
; #pragma unroll
;         for (int f = 0; f < 8; ++f) { const f32x16& S_ = (f >> 2) ? S1 : S0; const int q4 = f & 3; const float p3 = S_[4 * q4 + 3];
;             const float own = 2.f * (S_[4 * q4] + S_[4 * q4 + 1] + S_[4 * q4 + 2]) + p3;
;             const float inc = __builtin_bit_cast(float, __builtin_amdgcn_ds_bpermute(partner, __builtin_bit_cast(int, h ? prev3 : p3)));
;             irow[16 * ct + 2 * f + h] = own + inc;
;             prev3 = p3; }
;         if (h && ct < 3) __hip_atomic_fetch_add(irow + 16 * ct + 16, prev3, __ATOMIC_RELAXED, __HIP_MEMORY_SCOPE_WORKGROUP); }
;     u32x4 pk[4];
; #pragma unroll
;     for (int s2 = 0; s2 < 2; ++s2) { pk[s2].x = cvtpk(S0[8 * s2], S0[8 * s2 + 1]); pk[s2].y = cvtpk(S0[8 * s2 + 2], S0[8 * s2 + 3]); pk[s2].z = cvtpk(S0[8 * s2 + 4], S0[8 * s2 + 5]); pk[s2].w = cvtpk(S0[8 * s2 + 6], S0[8 * s2 + 7]);
;         pk[2 + s2].x = cvtpk(S1[8 * s2], S1[8 * s2 + 1]); pk[2 + s2].y = cvtpk(S1[8 * s2 + 2], S1[8 * s2 + 3]); pk[2 + s2].z = cvtpk(S1[8 * s2 + 4], S1[8 * s2 + 5]); pk[2 + s2].w = cvtpk(S1[8 * s2 + 6], S1[8 * s2 + 7]); }
;     __builtin_amdgcn_sched_barrier(0);
; #pragma unroll
;     for (int ks = 0; ks < 4; ++ks)
; #pragma unroll
;         for (int dt = 0; dt < 2; ++dt) st.O[dt] = __builtin_amdgcn_mfma_f32_32x32x16_bf16(vf[dt][ks], __builtin_bit_cast(bf16x8, pk[ks]), st.O[dt], 0, 0, 0);
;     __builtin_amdgcn_sched_barrier(0);
; __device__ __forceinline__ void att_unit_mfma(KArgs args, int b, int qb, LAS unsigned char* lds, int wave0, int lane0, int tid0) {
;     ...
;                 if (i == nw - 1) { const float lt = xhalf_sum(st.l); const float go = g2 / fmaxf(lt, 1e-30f);
; #pragma unroll
;                     for (int k = 0; k < 8; ++k) { OUTP[k] = cvtpk(st.O[0][2 * k] * go, st.O[0][2 * k + 1] * go); OUTP[8 + k] = cvtpk(st.O[1][2 * k] * go, st.O[1][2 * k + 1] * go); }
;                     att_state_reset(st); }
.LBB0_566:
	v_exp_f32_e32 v14, v96
	v_exp_f32_e32 v15, v80
	v_exp_f32_e32 v96, v97
	v_exp_f32_e32 v218, v81
	v_add_f32_e32 v80, 0, v14
	v_exp_f32_e32 v81, v98
	v_add_f32_e32 v97, 0, v15
	v_exp_f32_e32 v98, v82
	v_add_f32_e32 v80, v96, v80
	v_exp_f32_e32 v82, v99
	v_add_f32_e32 v97, v218, v97
	v_exp_f32_e32 v99, v83
	v_add_f32_e32 v80, v81, v80
	v_exp_f32_e32 v83, v100
	v_add_f32_e32 v97, v98, v97
	v_exp_f32_e32 v100, v84
	v_add_f32_e32 v80, v82, v80
	v_exp_f32_e32 v84, v101
	v_add_f32_e32 v97, v99, v97
	v_exp_f32_e32 v101, v85
	v_add_f32_e32 v80, v83, v80
	v_exp_f32_e32 v85, v102
	v_add_f32_e32 v97, v100, v97
	v_exp_f32_e32 v102, v86
	v_add_f32_e32 v80, v84, v80
	v_exp_f32_e32 v86, v103
	v_add_f32_e32 v97, v101, v97
	v_exp_f32_e32 v87, v87
	v_add_f32_e32 v80, v85, v80
	v_exp_f32_e32 v103, v104
	v_add_f32_e32 v97, v102, v97
	v_exp_f32_e32 v104, v88
	v_add_f32_e32 v80, v86, v80
	v_exp_f32_e32 v88, v105
	v_add_f32_e32 v97, v87, v97
	v_exp_f32_e32 v105, v89
	v_add_f32_e32 v80, v103, v80
	v_exp_f32_e32 v89, v106
	v_add_f32_e32 v97, v104, v97
	v_exp_f32_e32 v106, v90
	v_add_f32_e32 v80, v88, v80
	v_exp_f32_e32 v90, v107
	v_add_f32_e32 v97, v105, v97
	v_exp_f32_e32 v107, v91
	v_add_f32_e32 v80, v89, v80
	v_exp_f32_e32 v91, v108
	v_add_f32_e32 v97, v106, v97
	v_exp_f32_e32 v108, v92
	v_add_f32_e32 v80, v90, v80
	v_exp_f32_e32 v92, v109
	v_add_f32_e32 v97, v107, v97
	v_exp_f32_e32 v109, v93
	v_add_f32_e32 v80, v91, v80
	v_exp_f32_e32 v93, v110
	v_add_f32_e32 v97, v108, v97
	v_exp_f32_e32 v110, v94
	v_add_f32_e32 v80, v92, v80
	v_exp_f32_e32 v94, v111
	v_add_f32_e32 v97, v109, v97
	v_exp_f32_e32 v95, v95
	v_add_f32_e32 v80, v93, v80
	v_add_f32_e32 v97, v110, v97
	v_add_f32_e32 v80, v94, v80
	v_add_f32_e32 v97, v95, v97
	s_and_b64 s[24:25], s[28:29], s[24:25]
	v_add_f32_e32 v80, v80, v97
	v_add_f32_e32 v1, v1, v80
	s_add_i32 s0, s95, s40
	v_cvt_pk_bf16_f32 v80, v14, v96
	v_cvt_pk_bf16_f32 v81, v81, v82
	v_cvt_pk_bf16_f32 v82, v83, v84
	v_cvt_pk_bf16_f32 v83, v85, v86
	v_cvt_pk_bf16_f32 v84, v15, v218
	v_cvt_pk_bf16_f32 v85, v98, v99
	v_cvt_pk_bf16_f32 v86, v100, v101
	v_cvt_pk_bf16_f32 v87, v102, v87
	v_cvt_pk_bf16_f32 v88, v103, v88
	v_cvt_pk_bf16_f32 v89, v89, v90
	v_cvt_pk_bf16_f32 v90, v91, v92
	v_cvt_pk_bf16_f32 v91, v93, v94
	v_cvt_pk_bf16_f32 v92, v104, v105
	v_cvt_pk_bf16_f32 v93, v106, v107
	v_cvt_pk_bf16_f32 v94, v108, v109
	v_cvt_pk_bf16_f32 v95, v110, v95
	s_waitcnt lgkmcnt(14)
	v_mfma_f32_32x32x16_bf16 v[16:31], v[136:139], v[80:83], v[16:31]
	s_waitcnt lgkmcnt(6)
	v_mfma_f32_32x32x16_bf16 v[32:47], v[144:147], v[80:83], v[32:47]
	v_mfma_f32_32x32x16_bf16 v[16:31], v[128:131], v[88:91], v[16:31]
	s_waitcnt lgkmcnt(4)
	v_mfma_f32_32x32x16_bf16 v[32:47], v[140:143], v[88:91], v[32:47]
	v_mfma_f32_32x32x16_bf16 v[16:31], v[6:9], v[84:87], v[16:31]
	s_waitcnt lgkmcnt(2)
	v_mfma_f32_32x32x16_bf16 v[32:47], v[132:135], v[84:87], v[32:47]
	v_mfma_f32_32x32x16_bf16 v[16:31], v[2:5], v[92:95], v[16:31]
	s_waitcnt lgkmcnt(0)
	v_mfma_f32_32x32x16_bf16 v[32:47], v[10:13], v[92:95], v[32:47]
	s_cmp_lg_u32 s0, -8
	s_cbranch_scc1 .LBB0_568
	v_mov_b32_e32 v2, v1
	v_mov_b32_e32 v14, v0
	s_nop 0
	v_permlane32_swap_b32_e32 v1, v2
	v_mov_b32_e32 v15, v0
	v_add_f32_e32 v1, v1, v2
	v_max_f32_e32 v1, 0xda24260, v1
	v_div_scale_f32 v2, s[0:1], v1, v1, v182
	v_rcp_f32_e32 v3, v2
	v_mov_b32_e32 v7, v0
	v_mov_b32_e32 v8, v0
	v_mov_b32_e32 v9, v0
	v_fma_f32 v4, -v2, v3, 1.0
	v_fmac_f32_e32 v3, v4, v3
	v_div_scale_f32 v4, vcc, v182, v1, v182
	v_mul_f32_e32 v5, v4, v3
	v_fma_f32 v6, -v2, v5, v4
	v_fmac_f32_e32 v5, v6, v3
	v_fma_f32 v2, -v2, v5, v4
	v_div_fmas_f32 v2, v2, v3, v5
	v_div_fixup_f32 v2, v2, v1, v182
	v_pk_mul_f32 v[4:5], v[16:17], v[2:3] op_sel_hi:[1,0]
	v_mov_b32_e32 v1, v0
	v_cvt_pk_bf16_f32 v140, v4, v5
	v_pk_mul_f32 v[4:5], v[32:33], v[2:3] op_sel_hi:[1,0]
	v_mov_b32_e32 v6, v0
	v_cvt_pk_bf16_f32 v136, v4, v5
	v_pk_mul_f32 v[4:5], v[18:19], v[2:3] op_sel_hi:[1,0]
	v_mov_b32_e32 v10, v0
	v_cvt_pk_bf16_f32 v139, v4, v5
	v_pk_mul_f32 v[4:5], v[34:35], v[2:3] op_sel_hi:[1,0]
	v_mov_b32_e32 v11, v0
	v_cvt_pk_bf16_f32 v135, v4, v5
	v_pk_mul_f32 v[4:5], v[20:21], v[2:3] op_sel_hi:[1,0]
	v_mov_b32_e32 v12, v0
	v_cvt_pk_bf16_f32 v138, v4, v5
	v_pk_mul_f32 v[4:5], v[36:37], v[2:3] op_sel_hi:[1,0]
	v_mov_b32_e32 v13, v0
	v_cvt_pk_bf16_f32 v133, v4, v5
	v_pk_mul_f32 v[4:5], v[22:23], v[2:3] op_sel_hi:[1,0]
	v_mov_b32_e32 v226, 0
	v_cvt_pk_bf16_f32 v137, v4, v5
	v_pk_mul_f32 v[4:5], v[38:39], v[2:3] op_sel_hi:[1,0]
	s_or_b64 s[24:25], s[24:25], exec
	v_cvt_pk_bf16_f32 v131, v4, v5
	v_pk_mul_f32 v[4:5], v[24:25], v[2:3] op_sel_hi:[1,0]
	s_nop 0
	v_cvt_pk_bf16_f32 v134, v4, v5
	v_pk_mul_f32 v[4:5], v[40:41], v[2:3] op_sel_hi:[1,0]
	s_nop 0
	v_cvt_pk_bf16_f32 v129, v4, v5
	v_pk_mul_f32 v[4:5], v[26:27], v[2:3] op_sel_hi:[1,0]
	s_nop 0
	v_cvt_pk_bf16_f32 v132, v4, v5
	v_pk_mul_f32 v[4:5], v[42:43], v[2:3] op_sel_hi:[1,0]
	s_nop 0
	v_cvt_pk_bf16_f32 v111, v4, v5
	v_pk_mul_f32 v[4:5], v[28:29], v[2:3] op_sel_hi:[1,0]
	s_nop 0
	v_cvt_pk_bf16_f32 v130, v4, v5
	v_pk_mul_f32 v[4:5], v[44:45], v[2:3] op_sel_hi:[1,0]
	s_nop 0
	v_cvt_pk_bf16_f32 v110, v4, v5
	v_pk_mul_f32 v[4:5], v[30:31], v[2:3] op_sel_hi:[1,0]
	v_pk_mul_f32 v[2:3], v[46:47], v[2:3] op_sel_hi:[1,0]
	v_cvt_pk_bf16_f32 v128, v4, v5
	v_cvt_pk_bf16_f32 v101, v2, v3
	v_mov_b32_e32 v2, v0
	v_mov_b32_e32 v3, v0
	v_mov_b32_e32 v4, v0
	v_mov_b32_e32 v5, v0
	v_mov_b64_e32 v[30:31], v[14:15]
	v_mov_b64_e32 v[46:47], v[14:15]
	v_mov_b64_e32 v[28:29], v[12:13]
	v_mov_b64_e32 v[26:27], v[10:11]
	v_mov_b64_e32 v[24:25], v[8:9]
	v_mov_b64_e32 v[22:23], v[6:7]
	v_mov_b64_e32 v[20:21], v[4:5]
	v_mov_b64_e32 v[18:19], v[2:3]
	v_mov_b64_e32 v[16:17], v[0:1]
	v_mov_b64_e32 v[44:45], v[12:13]
	v_mov_b64_e32 v[42:43], v[10:11]
	v_mov_b64_e32 v[40:41], v[8:9]
	v_mov_b64_e32 v[38:39], v[6:7]
	v_mov_b64_e32 v[36:37], v[4:5]
	v_mov_b64_e32 v[34:35], v[2:3]
	v_mov_b64_e32 v[32:33], v[0:1]
	v_mov_b32_e32 v1, 0
	s_branch .LBB0_569

; __device__ __forceinline__ unsigned cvtpk(float lo, float hi) { f32x2_t v = {lo, hi}; bf16x2_t b = __builtin_convertvector(v, bf16x2_t); return __builtin_bit_cast(unsigned, b); }
;     ...
;     for (int i = 0; i < 16; ++i) { S0[i] = __builtin_amdgcn_exp2f(S0[i]); S1[i] = __builtin_amdgcn_exp2f(S1[i]); ps += S0[i]; asm volatile("" : "+v"(ps)); pt += S1[i]; asm volatile("" : "+v"(pt)); }
;     st.l += ps + pt;
;     if (IMP) {
;         float prev3 = 0.f; const int partner = (lane ^ 32) << 2;
; #pragma unroll
;         for (int f = 0; f < 8; ++f) { const f32x16& S_ = (f >> 2) ? S1 : S0; const int q4 = f & 3; const float p3 = S_[4 * q4 + 3];
;             const float own = 2.f * (S_[4 * q4] + S_[4 * q4 + 1] + S_[4 * q4 + 2]) + p3;
;             const float inc = __builtin_bit_cast(float, __builtin_amdgcn_ds_bpermute(partner, __builtin_bit_cast(int, h ? prev3 : p3)));
;             irow[16 * ct + 2 * f + h] = own + inc;
;             prev3 = p3; }
;         if (h && ct < 3) __hip_atomic_fetch_add(irow + 16 * ct + 16, prev3, __ATOMIC_RELAXED, __HIP_MEMORY_SCOPE_WORKGROUP); }
;     u32x4 pk[4];
; #pragma unroll
;     for (int s2 = 0; s2 < 2; ++s2) { pk[s2].x = cvtpk(S0[8 * s2], S0[8 * s2 + 1]); pk[s2].y = cvtpk(S0[8 * s2 + 2], S0[8 * s2 + 3]); pk[s2].z = cvtpk(S0[8 * s2 + 4], S0[8 * s2 + 5]); pk[s2].w = cvtpk(S0[8 * s2 + 6], S0[8 * s2 + 7]);
;         pk[2 + s2].x = cvtpk(S1[8 * s2], S1[8 * s2 + 1]); pk[2 + s2].y = cvtpk(S1[8 * s2 + 2], S1[8 * s2 + 3]); pk[2 + s2].z = cvtpk(S1[8 * s2 + 4], S1[8 * s2 + 5]); pk[2 + s2].w = cvtpk(S1[8 * s2 + 6], S1[8 * s2 + 7]); }
;     __builtin_amdgcn_sched_barrier(0);
; #pragma unroll
;     for (int ks = 0; ks < 4; ++ks)
; #pragma unroll
;         for (int dt = 0; dt < 2; ++dt) st.O[dt] = __builtin_amdgcn_mfma_f32_32x32x16_bf16(vf[dt][ks], __builtin_bit_cast(bf16x8, pk[ks]), st.O[dt], 0, 0, 0);
;     __builtin_amdgcn_sched_barrier(0);
.LBB0_580:
	v_exp_f32_e32 v56, v106
	v_exp_f32_e32 v14, v78
	v_exp_f32_e32 v57, v105
	v_exp_f32_e32 v58, v77
	v_add_f32_e32 v59, 0, v56
	v_exp_f32_e32 v60, v104
	v_add_f32_e32 v61, 0, v14
	v_add_f32_e32 v62, v59, v57
	v_exp_f32_e32 v59, v76
	v_exp_f32_e32 v73, v73
	v_add_f32_e32 v61, v61, v58
	v_add_f32_e32 v63, v60, v62
	v_exp_f32_e32 v62, v103
	v_exp_f32_e32 v72, v72
	v_add_f32_e32 v76, v59, v61
	v_exp_f32_e32 v61, v75
	v_add_f32_e32 v77, v62, v63
	v_exp_f32_e32 v75, v102
	v_exp_f32_e32 v63, v74
	v_exp_f32_e32 v74, v101
	v_add_f32_e32 v76, v61, v76
	v_exp_f32_e32 v69, v69
	v_add_f32_e32 v77, v75, v77
	v_add_f32_e32 v78, v63, v76
	v_exp_f32_e32 v76, v100
	v_exp_f32_e32 v55, v55
	v_add_f32_e32 v77, v74, v77
	v_add_f32_e32 v78, v73, v78
	v_add_f32_e32 v79, v76, v77
	v_exp_f32_e32 v77, v70
	v_exp_f32_e32 v70, v71
	v_exp_f32_e32 v68, v68
	v_add_f32_e32 v78, v72, v78
	v_add_f32_e32 v71, v77, v79
	v_exp_f32_e32 v54, v54
	v_add_f32_e32 v78, v70, v78
	v_add_f32_e32 v71, v69, v71
	v_exp_f32_e32 v67, v67
	v_exp_f32_e32 v53, v53
	v_add_f32_e32 v78, v55, v78
	v_add_f32_e32 v71, v68, v71
	v_exp_f32_e32 v66, v66
	v_exp_f32_e32 v52, v52
	v_add_f32_e32 v78, v54, v78
	v_add_f32_e32 v71, v67, v71
	v_exp_f32_e32 v65, v65
	v_exp_f32_e32 v64, v64
	v_add_f32_e32 v78, v53, v78
	v_add_f32_e32 v71, v66, v71
	v_exp_f32_e32 v51, v51
	v_add_f32_e32 v78, v52, v78
	v_add_f32_e32 v71, v65, v71
	v_exp_f32_e32 v50, v50
	v_cndmask_b32_e64 v100, 0, v62, s[20:21]
	v_add_f32_e32 v79, v64, v71
	v_exp_f32_e32 v71, v15
	ds_bpermute_b32 v100, v203, v100
	v_add_f32_e32 v78, v51, v78
	v_exp_f32_e32 v15, v49
	v_exp_f32_e32 v49, v1
	v_add_f32_e32 v102, v56, v57
	v_add_f32_e32 v78, v50, v78
	v_exp_f32_e32 v48, v48
	v_add_f32_e32 v102, v60, v102
	v_add_f32_e32 v79, v71, v79
	v_fma_f32 v102, 2.0, v102, v62
	v_add_f32_e32 v78, v15, v78
	s_waitcnt lgkmcnt(0)
	v_add_f32_e32 v100, v102, v100
	v_cndmask_b32_e64 v102, v62, v77, s[20:21]
	v_add_f32_e32 v1, v49, v79
	v_add_u32_e32 v79, s42, v222
	ds_bpermute_b32 v102, v203, v102
	v_add_f32_e32 v78, v48, v78
	v_add_u32_e32 v101, 0x10000, v79
	ds_write_b32 v101, v100
	v_add_f32_e32 v100, v75, v74
	v_add_f32_e32 v100, v76, v100
	v_fma_f32 v100, 2.0, v100, v77
	s_waitcnt lgkmcnt(1)
	v_add_f32_e32 v100, v100, v102
	v_cndmask_b32_e64 v102, v77, v66, s[20:21]
	ds_bpermute_b32 v102, v203, v102
	v_add_u32_e32 v101, 0x10008, v79
	ds_write_b32 v101, v100
	v_add_f32_e32 v100, v69, v68
	v_add_f32_e32 v100, v67, v100
	v_fma_f32 v100, 2.0, v100, v66
	s_waitcnt lgkmcnt(1)
	v_add_f32_e32 v100, v100, v102
	v_cndmask_b32_e64 v102, v66, v49, s[20:21]
	ds_bpermute_b32 v102, v203, v102
	v_add_u32_e32 v101, 0x10010, v79
	ds_write_b32 v101, v100
	v_add_f32_e32 v100, v65, v64
	v_add_f32_e32 v100, v71, v100
	v_fma_f32 v100, 2.0, v100, v49
	s_waitcnt lgkmcnt(1)
	v_add_f32_e32 v100, v100, v102
	v_cndmask_b32_e64 v102, v49, v61, s[20:21]
	ds_bpermute_b32 v102, v203, v102
	v_add_u32_e32 v101, 0x10018, v79
	ds_write_b32 v101, v100
	v_add_f32_e32 v100, v14, v58
	v_add_f32_e32 v100, v59, v100
	v_fma_f32 v100, 2.0, v100, v61
	s_waitcnt lgkmcnt(1)
	v_add_f32_e32 v100, v100, v102
	v_cndmask_b32_e64 v102, v61, v70, s[20:21]
	ds_bpermute_b32 v102, v203, v102
	v_add_u32_e32 v101, 0x10020, v79
	ds_write_b32 v101, v100
	v_add_f32_e32 v100, v63, v73
	v_add_f32_e32 v100, v72, v100
	v_fma_f32 v100, 2.0, v100, v70
	s_waitcnt lgkmcnt(1)
	v_add_f32_e32 v100, v100, v102
	v_cndmask_b32_e64 v102, v70, v52, s[20:21]
	ds_bpermute_b32 v102, v203, v102
	v_add_u32_e32 v101, 0x10028, v79
	ds_write_b32 v101, v100
	v_add_f32_e32 v100, v55, v54
	v_add_f32_e32 v100, v53, v100
	v_fma_f32 v100, 2.0, v100, v52
	s_waitcnt lgkmcnt(1)
	v_add_f32_e32 v100, v100, v102
	v_cndmask_b32_e64 v102, v52, v48, s[20:21]
	ds_bpermute_b32 v102, v203, v102
	v_add_u32_e32 v101, 0x10030, v79
	ds_write_b32 v101, v100
	v_add_f32_e32 v100, v51, v50
	v_add_f32_e32 v100, v15, v100
	s_cmp_lt_i32 s41, 3
	v_fma_f32 v100, 2.0, v100, v48
	s_cselect_b64 s[0:1], -1, 0
	s_waitcnt lgkmcnt(1)
	v_add_f32_e32 v100, v100, v102
	v_add_u32_e32 v79, 0x10038, v79
	s_and_b64 s[0:1], s[22:23], s[0:1]
	ds_write_b32 v79, v100
	s_and_saveexec_b64 s[26:27], s[0:1]
	v_add_u32_e32 v79, s42, v221
	v_add_u32_e32 v79, 0x10040, v79
	ds_add_f32 v79, v48
	s_or_b64 exec, exec, s[26:27]
	v_add_f32_e32 v1, v1, v78
	v_add_f32_e32 v1, v224, v1
	v_cvt_pk_bf16_f32 v100, v56, v57
	v_cvt_pk_bf16_f32 v101, v60, v62
	v_cvt_pk_bf16_f32 v56, v14, v58
	v_cvt_pk_bf16_f32 v57, v59, v61
	v_cvt_pk_bf16_f32 v58, v63, v73
	v_cvt_pk_bf16_f32 v59, v72, v70
	v_cvt_pk_bf16_f32 v60, v69, v68
	v_cvt_pk_bf16_f32 v61, v67, v66
	v_cvt_pk_bf16_f32 v62, v65, v64
	v_cvt_pk_bf16_f32 v63, v71, v49
	s_add_i32 s0, s78, s40
	v_cvt_pk_bf16_f32 v102, v75, v74
	v_cvt_pk_bf16_f32 v103, v76, v77
	v_cvt_pk_bf16_f32 v104, v55, v54
	v_cvt_pk_bf16_f32 v105, v53, v52
	v_cvt_pk_bf16_f32 v106, v51, v50
	v_cvt_pk_bf16_f32 v107, v15, v48
	v_mfma_f32_32x32x16_bf16 v[16:31], v[88:91], v[100:103], v[16:31]
	v_mfma_f32_32x32x16_bf16 v[32:47], v[96:99], v[100:103], v[32:47]
	v_mfma_f32_32x32x16_bf16 v[16:31], v[80:83], v[60:63], v[16:31]
	v_mfma_f32_32x32x16_bf16 v[32:47], v[92:95], v[60:63], v[32:47]
	v_mfma_f32_32x32x16_bf16 v[16:31], v[6:9], v[56:59], v[16:31]
	v_mfma_f32_32x32x16_bf16 v[32:47], v[84:87], v[56:59], v[32:47]
	v_mfma_f32_32x32x16_bf16 v[16:31], v[2:5], v[104:107], v[16:31]
	s_nop 0
	v_mfma_f32_32x32x16_bf16 v[32:47], v[10:13], v[104:107], v[32:47]
	s_cmp_lg_u32 s0, -8
	s_cbranch_scc1 .LBB0_586
; #define LAS __attribute__((address_space(3)))
; __device__ __forceinline__ unsigned cvtpk(float lo, float hi) { f32x2_t v = {lo, hi}; bf16x2_t b = __builtin_convertvector(v, bf16x2_t); return __builtin_bit_cast(unsigned, b); }
; __device__ __forceinline__ float xhalf_sum(float m) { float a, b; xhalf_pair(m, a, b); return a + b; }
; __device__ __forceinline__ void att_unit_mfma(KArgs args, int b, int qb, LAS unsigned char* lds, int wave0, int lane0, int tid0) {
;     ...
;                 if (i == nA - 1) { const float lt = xhalf_sum(st.l); il_c = 1.f / fmaxf(lt, 1e-30f); const float go = g0 * il_c;
;                     if (h == 0) ((LAS float*)(lds + ATT_SC))[r * 64 + tl] = il_c;
; #pragma unroll
;                     for (int k = 0; k < 8; ++k) { OUTP[k] = cvtpk(bflo(OUTP[k]) + st.O[0][2 * k] * go, bfhi(OUTP[k]) + st.O[0][2 * k + 1] * go); OUTP[8 + k] = cvtpk(bflo(OUTP[8 + k]) + st.O[1][2 * k] * go, bfhi(OUTP[8 + k]) + st.O[1][2 * k + 1] * go); } }
	v_mov_b32_e32 v2, v1
	v_mov_b32_e32 v3, v1
	s_nop 1
	v_permlane32_swap_b32_e32 v3, v2
	s_nop 0
	v_add_f32_e32 v2, v3, v2
	v_max_f32_e32 v2, 0xda24260, v2
	v_div_scale_f32 v3, s[0:1], v2, v2, 1.0
	v_rcp_f32_e32 v4, v3
	s_nop 0
	v_fma_f32 v5, -v3, v4, 1.0
	v_fmac_f32_e32 v4, v5, v4
	v_div_scale_f32 v5, vcc, 1.0, v2, 1.0
	v_mul_f32_e32 v6, v5, v4
	v_fma_f32 v7, -v3, v6, v5
	v_fmac_f32_e32 v6, v7, v4
	v_fma_f32 v3, -v3, v6, v5
	v_div_fmas_f32 v3, v3, v4, v6
	v_div_fixup_f32 v2, v3, v2, 1.0
	s_and_saveexec_b64 s[26:27], s[20:21]
	ds_write_b32 v204, v2
	s_or_b64 exec, exec, s[26:27]
	v_mul_f32_e32 v2, v181, v2
	v_lshlrev_b32_e32 v4, 16, v160
	v_and_b32_e32 v5, 0xffff0000, v160
	v_pk_fma_f32 v[4:5], v[16:17], v[2:3], v[4:5] op_sel_hi:[1,0,1]
	s_nop 0
	v_cvt_pk_bf16_f32 v160, v4, v5
	v_lshlrev_b32_e32 v4, 16, v150
	v_and_b32_e32 v5, 0xffff0000, v150
	v_pk_fma_f32 v[4:5], v[32:33], v[2:3], v[4:5] op_sel_hi:[1,0,1]
	s_nop 0
	v_cvt_pk_bf16_f32 v150, v4, v5
	v_lshlrev_b32_e32 v4, 16, v161
	v_and_b32_e32 v5, 0xffff0000, v161
	v_pk_fma_f32 v[4:5], v[18:19], v[2:3], v[4:5] op_sel_hi:[1,0,1]
	s_nop 0
	v_cvt_pk_bf16_f32 v161, v4, v5
	v_lshlrev_b32_e32 v4, 16, v151
	v_and_b32_e32 v5, 0xffff0000, v151
	v_pk_fma_f32 v[4:5], v[34:35], v[2:3], v[4:5] op_sel_hi:[1,0,1]
	s_nop 0
	v_cvt_pk_bf16_f32 v151, v4, v5
	v_lshlrev_b32_e32 v4, 16, v148
	v_and_b32_e32 v5, 0xffff0000, v148
	v_pk_fma_f32 v[4:5], v[20:21], v[2:3], v[4:5] op_sel_hi:[1,0,1]
	s_nop 0
	v_cvt_pk_bf16_f32 v148, v4, v5
	v_lshlrev_b32_e32 v4, 16, v152
	v_and_b32_e32 v5, 0xffff0000, v152
	v_pk_fma_f32 v[4:5], v[36:37], v[2:3], v[4:5] op_sel_hi:[1,0,1]
	s_nop 0
	v_cvt_pk_bf16_f32 v152, v4, v5
	v_lshlrev_b32_e32 v4, 16, v149
	v_and_b32_e32 v5, 0xffff0000, v149
	v_pk_fma_f32 v[4:5], v[22:23], v[2:3], v[4:5] op_sel_hi:[1,0,1]
	s_nop 0
	v_cvt_pk_bf16_f32 v149, v4, v5
	v_lshlrev_b32_e32 v4, 16, v153
	v_and_b32_e32 v5, 0xffff0000, v153
	v_pk_fma_f32 v[4:5], v[38:39], v[2:3], v[4:5] op_sel_hi:[1,0,1]
	s_nop 0
	v_cvt_pk_bf16_f32 v153, v4, v5
	v_lshlrev_b32_e32 v4, 16, v158
	v_and_b32_e32 v5, 0xffff0000, v158
	v_pk_fma_f32 v[4:5], v[24:25], v[2:3], v[4:5] op_sel_hi:[1,0,1]
	s_nop 0
	v_cvt_pk_bf16_f32 v158, v4, v5
	v_lshlrev_b32_e32 v4, 16, v154
	v_and_b32_e32 v5, 0xffff0000, v154
	v_pk_fma_f32 v[4:5], v[40:41], v[2:3], v[4:5] op_sel_hi:[1,0,1]
	s_nop 0
	v_cvt_pk_bf16_f32 v154, v4, v5
	v_lshlrev_b32_e32 v4, 16, v159
	v_and_b32_e32 v5, 0xffff0000, v159
	v_pk_fma_f32 v[4:5], v[26:27], v[2:3], v[4:5] op_sel_hi:[1,0,1]
	s_nop 0
	v_cvt_pk_bf16_f32 v159, v4, v5
	v_lshlrev_b32_e32 v4, 16, v155
	v_and_b32_e32 v5, 0xffff0000, v155
	v_pk_fma_f32 v[4:5], v[42:43], v[2:3], v[4:5] op_sel_hi:[1,0,1]
	s_nop 0
	v_cvt_pk_bf16_f32 v155, v4, v5
	v_lshlrev_b32_e32 v4, 16, v162
	v_and_b32_e32 v5, 0xffff0000, v162
	v_pk_fma_f32 v[4:5], v[28:29], v[2:3], v[4:5] op_sel_hi:[1,0,1]
	s_nop 0
	v_cvt_pk_bf16_f32 v162, v4, v5
	v_lshlrev_b32_e32 v4, 16, v156
	v_and_b32_e32 v5, 0xffff0000, v156
	v_pk_fma_f32 v[4:5], v[44:45], v[2:3], v[4:5] op_sel_hi:[1,0,1]
	s_nop 0
	v_cvt_pk_bf16_f32 v156, v4, v5
	v_lshlrev_b32_e32 v4, 16, v163
	v_and_b32_e32 v5, 0xffff0000, v163
	v_pk_fma_f32 v[4:5], v[30:31], v[2:3], v[4:5] op_sel_hi:[1,0,1]
	s_nop 0
	v_cvt_pk_bf16_f32 v163, v4, v5
	v_lshlrev_b32_e32 v4, 16, v157
	v_and_b32_e32 v5, 0xffff0000, v157
	v_pk_fma_f32 v[2:3], v[46:47], v[2:3], v[4:5] op_sel_hi:[1,0,1]
	s_nop 0
	v_cvt_pk_bf16_f32 v157, v2, v3

; #define LAS __attribute__((address_space(3)))
; __device__ __forceinline__ unsigned cvtpk(float lo, float hi) { f32x2_t v = {lo, hi}; bf16x2_t b = __builtin_convertvector(v, bf16x2_t); return __builtin_bit_cast(unsigned, b); }
; __device__ __forceinline__ float xhalf_sum(float m) { float a, b; xhalf_pair(m, a, b); return a + b; }
; #define ATT_WAIT_BAR_PD() asm volatile("s_waitcnt vmcnt(4) lgkmcnt(0)\n\ts_barrier" ::: "memory")
; __device__ __forceinline__ void att_unit_mfma(KArgs args, int b, int qb, LAS unsigned char* lds, int wave0, int lane0, int tid0) {
;     ...
; #pragma unroll 1
;         for (int i = 0; i < nA; ++i) {
;             ATT_WAIT_BAR_PD();
;             ATT_STAGE_A(i + ATT_PD);
;             const LAS unsigned char* Kb = lds + (i & 3) * 16384; const LAS unsigned char* Vb = Kb + 8192;
;             if (i < nw) {
;                 const int j = qb - i;
;                 att_qk64(Kb, qf, slope2, slope2 * (float)(64 * j) - st.m, rq, h, Sa, Sb);
;                 att_softmax_pv64<false>((j == qb) || (j == qb - 8), Vb, (j == qb - 8) ? tl : -1, (j == qb) ? tl : 63, Sa, Sb, st, h, lane);
;                 if (i == nw - 1) { const float lt = xhalf_sum(st.l); const float go = g2 / fmaxf(lt, 1e-30f);
; #pragma unroll
;                     for (int k = 0; k < 8; ++k) { OUTP[k] = cvtpk(st.O[0][2 * k] * go, st.O[0][2 * k + 1] * go); OUTP[8 + k] = cvtpk(st.O[1][2 * k] * go, st.O[1][2 * k + 1] * go); }
;                     att_state_reset(st); }
;             } else {
;                 const int ct = nc - 1 - (i - nw);
;                 att_qk64(Kb, qf, sF, sF * (float)(64 * ct) - st.m, rq, h, Sa, Sb);
;                 att_softmax_pv64<true>(true, Vb, -1, nmax_t - 64 * ct, Sa, Sb, st, h, lane, irow, ct);
;                 if (i == nA - 1) { const float lt = xhalf_sum(st.l); il_c = 1.f / fmaxf(lt, 1e-30f); const float go = g0 * il_c;
;                     if (h == 0) ((LAS float*)(lds + ATT_SC))[r * 64 + tl] = il_c;
; #pragma unroll
;                     for (int k = 0; k < 8; ++k) { OUTP[k] = cvtpk(bflo(OUTP[k]) + st.O[0][2 * k] * go, bfhi(OUTP[k]) + st.O[0][2 * k + 1] * go); OUTP[8 + k] = cvtpk(bflo(OUTP[8 + k]) + st.O[1][2 * k] * go, bfhi(OUTP[8 + k]) + st.O[1][2 * k + 1] * go); } }
;             }
;         }
.LBB0_587:
	s_add_i32 s40, s40, 1
	s_sub_i32 s42, s42, 64
	s_add_i32 s41, s41, -1
	s_addk_i32 s39, 0x4000
	s_add_i32 s0, s78, s40
	s_cmp_eq_u32 s0, -7
	v_add_u32_e32 v205, 64, v205
	s_cbranch_scc1 .LBB0_590
	s_mov_b64 s[28:29], s[24:25]
	v_mov_b32_e32 v149, v137
	v_mov_b32_e32 v148, v138
	v_mov_b32_e32 v161, v139
	v_mov_b32_e32 v160, v140
	v_mov_b32_e32 v158, v134
	v_mov_b32_e32 v159, v132
	v_mov_b32_e32 v162, v130
	v_mov_b32_e32 v163, v128
	v_mov_b32_e32 v150, v136
	v_mov_b32_e32 v151, v135
	v_mov_b32_e32 v152, v133
	v_mov_b32_e32 v153, v131
	v_mov_b32_e32 v154, v129
	v_mov_b32_e32 v155, v111
	v_mov_b32_e32 v156, v110
	v_mov_b32_e32 v157, v101
	v_mov_b32_e32 v225, v226
	v_mov_b32_e32 v224, v1
	s_branch .LBB0_553
